# outproj K loop: counted LDS waits (lgkmcnt(1) for the MFMA that needs only the first of two ds_reads, wait for the second moved to its consumer)
# baseline (speedup 1.0000x reference)
_Z9k_outprojPKDF16_S0_PKfPf:
	s_load_dwordx8 s[4:11], s[0:1], 0x0
	s_and_b32 s12, s2, 7
	s_lshr_b32 s13, s2, 3
	s_mul_i32 s14, s12, 43
	s_min_u32 s12, s12, 4
	s_add_u32 s14, s14, s12
	s_add_u32 s2, s14, s13
	v_and_b32_e32 v3, 31, v0
	s_and_b32 s1, s2, 3
	v_lshlrev_b32_e32 v1, 2, v3
	v_lshl_or_b32 v66, s1, 9, v1
	s_waitcnt lgkmcnt(0)
	global_load_dword v50, v66, s[8:9]
	global_load_dword v34, v66, s[8:9] offset:128
	global_load_dword v18, v66, s[8:9] offset:256
	v_lshrrev_b32_e32 v4, 6, v0
	v_bfe_u32 v1, v0, 3, 3
	s_lshl_b32 s0, s2, 5
	v_lshl_or_b32 v2, v4, 3, v1
	s_and_b32 s0, s0, 0x7fffff80
	v_lshrrev_b32_e32 v5, 1, v2
	v_or_b32_e32 v7, s0, v2
	v_lshlrev_b32_e32 v8, 9, v2
	v_or_b32_e32 v9, 32, v2
	v_or_b32_e32 v10, 64, v2
	v_or_b32_e32 v2, 0x60, v2
	v_xor_b32_e32 v5, v5, v0
	v_or_b32_e32 v14, s0, v2
	v_lshlrev_b32_e32 v15, 9, v2
	v_lshlrev_b32_e32 v2, 3, v5
	v_and_b32_e32 v5, 56, v2
	global_load_dword v2, v66, s[8:9] offset:384
	v_lshlrev_b32_e32 v1, 5, v4
	v_or_b32_e32 v11, v1, v3
	v_lshlrev_b32_e32 v104, 7, v11
	v_lshlrev_b32_e32 v11, 10, v4
	v_mov_b32_e32 v67, 0
	s_lshl_b32 s1, s1, 16
	v_min_u32_e32 v7, 0x2b17, v7
	v_or_b32_e32 v12, s0, v9
	v_lshlrev_b32_e32 v9, 9, v9
	v_or_b32_e32 v13, s0, v10
	v_lshlrev_b32_e32 v10, 9, v10
	v_lshlrev_b32_e32 v16, 1, v5
	v_readfirstlane_b32 s9, v11
	v_or3_b32 v8, v8, s1, v5
	v_or3_b32 v9, v9, s1, v5
	v_or3_b32 v10, v10, s1, v5
	v_or3_b32 v15, v15, s1, v5
	v_lshl_or_b32 v4, v7, 10, v16
	v_mov_b32_e32 v5, v67
	s_mov_b32 m0, s9
	v_lshl_add_u64 v[68:69], s[4:5], 0, v[4:5]
	global_load_lds_dwordx4 v4, s[4:5]
	v_lshlrev_b32_e32 v4, 1, v8
	v_min_u32_e32 v12, 0x2b17, v12
	v_lshl_add_u64 v[70:71], s[6:7], 0, v[4:5]
	v_or_b32_e32 v4, 0x4000, v11
	v_min_u32_e32 v13, 0x2b17, v13
	v_readfirstlane_b32 s12, v4
	v_lshl_or_b32 v4, v12, 10, v16
	v_lshl_add_u64 v[72:73], s[4:5], 0, v[4:5]
	v_or_b32_e32 v5, 0x1000, v11
	s_mov_b32 m0, s12
	v_readfirstlane_b32 s13, v5
	global_load_lds_dwordx4 v[70:71], off
	s_mov_b32 m0, s13
	v_mov_b32_e32 v5, v67
	global_load_lds_dwordx4 v4, s[4:5]
	v_lshlrev_b32_e32 v4, 1, v9
	v_lshl_add_u64 v[74:75], s[6:7], 0, v[4:5]
	v_or_b32_e32 v4, 0x5000, v11
	v_min_u32_e32 v14, 0x2b17, v14
	v_readfirstlane_b32 s14, v4
	v_lshl_or_b32 v4, v13, 10, v16
	v_lshl_add_u64 v[76:77], s[4:5], 0, v[4:5]
	v_or_b32_e32 v5, 0x2000, v11
	s_mov_b32 m0, s14
	v_readfirstlane_b32 s15, v5
	global_load_lds_dwordx4 v[74:75], off
	s_mov_b32 m0, s15
	v_mov_b32_e32 v5, v67
	global_load_lds_dwordx4 v4, s[4:5]
	v_lshlrev_b32_e32 v4, 1, v10
	v_lshl_add_u64 v[78:79], s[6:7], 0, v[4:5]
	v_or_b32_e32 v4, 0x6000, v11
	v_or_b32_e32 v7, 0x8000, v11
	v_readfirstlane_b32 s16, v4
	v_lshl_or_b32 v4, v14, 10, v16
	v_lshl_add_u64 v[80:81], s[4:5], 0, v[4:5]
	v_or_b32_e32 v5, 0x3000, v11
	s_mov_b32 m0, s16
	v_readfirstlane_b32 s17, v5
	global_load_lds_dwordx4 v[78:79], off
	s_mov_b32 m0, s17
	v_mov_b32_e32 v5, v67
	global_load_lds_dwordx4 v4, s[4:5]
	v_lshlrev_b32_e32 v4, 1, v15
	v_lshl_add_u64 v[82:83], s[6:7], 0, v[4:5]
	v_or_b32_e32 v4, 0x7000, v11
	s_mov_b64 s[20:21], 0x80
	v_readfirstlane_b32 s18, v4
	s_mov_b32 m0, s18
	v_readfirstlane_b32 s1, v7
	v_or_b32_e32 v7, 0xc000, v11
	global_load_lds_dwordx4 v[82:83], off
	v_lshl_add_u64 v[4:5], v[68:69], 0, s[20:21]
	s_mov_b32 m0, s1
	v_readfirstlane_b32 s2, v7
	v_or_b32_e32 v7, 0x9000, v11
	s_waitcnt vmcnt(0) lgkmcnt(0)
	s_barrier
	global_load_lds_dwordx4 v[4:5], off
	v_lshl_add_u64 v[4:5], v[70:71], 0, s[20:21]
	s_mov_b32 m0, s2
	v_readfirstlane_b32 s3, v7
	v_or_b32_e32 v7, 0xd000, v11
	global_load_lds_dwordx4 v[4:5], off
	v_lshl_add_u64 v[4:5], v[72:73], 0, s[20:21]
	s_mov_b32 m0, s3
	v_readfirstlane_b32 s4, v7
	v_or_b32_e32 v7, 0xa000, v11
	global_load_lds_dwordx4 v[4:5], off
	v_lshl_add_u64 v[4:5], v[74:75], 0, s[20:21]
	s_mov_b32 m0, s4
	v_readfirstlane_b32 s5, v7
	v_or_b32_e32 v7, 0xe000, v11
	global_load_lds_dwordx4 v[4:5], off
	v_lshl_add_u64 v[4:5], v[76:77], 0, s[20:21]
	s_mov_b32 m0, s5
	v_readfirstlane_b32 s6, v7
	v_or_b32_e32 v7, 0xb000, v11
	global_load_lds_dwordx4 v[4:5], off
	v_lshl_add_u64 v[4:5], v[78:79], 0, s[20:21]
	s_mov_b32 m0, s6
	v_readfirstlane_b32 s7, v7
	v_or_b32_e32 v7, 0xf000, v11
	global_load_lds_dwordx4 v[4:5], off
	v_lshl_add_u64 v[4:5], v[80:81], 0, s[20:21]
	s_mov_b32 m0, s7
	v_readfirstlane_b32 s8, v7
	v_lshrrev_b32_e32 v6, 1, v0
	v_bfe_u32 v84, v0, 5, 1
	global_load_lds_dwordx4 v[4:5], off
	v_lshl_add_u64 v[4:5], v[82:83], 0, s[20:21]
	s_mov_b32 m0, s8
	v_lshlrev_b32_e32 v105, 7, v3
	global_load_lds_dwordx4 v[4:5], off
	v_bitop3_b32 v4, v84, v6, 7 bitop3:0x78
	v_lshlrev_b32_e32 v4, 4, v4
	v_or_b32_e32 v86, v104, v4
	ds_read_b128 v[90:93], v86
	v_or_b32_e32 v85, v105, v4
	ds_read_b128 v[94:97], v85 offset:24576
	ds_read_b128 v[6:9], v85 offset:16384
	ds_read_b128 v[10:13], v85 offset:20480
	v_bfe_u32 v106, v0, 1, 3
	v_bitop3_b32 v0, v84, v106, 2 bitop3:0x36
	v_mov_b32_e32 v19, v18
	v_mov_b32_e32 v20, v18
	v_mov_b32_e32 v21, v18
	v_mov_b32_e32 v22, v18
	v_mov_b32_e32 v23, v18
	v_mov_b32_e32 v24, v18
	v_mov_b32_e32 v25, v18
	v_mov_b32_e32 v26, v18
	v_mov_b32_e32 v27, v18
	v_mov_b32_e32 v28, v18
	v_mov_b32_e32 v29, v18
	v_mov_b32_e32 v30, v18
	v_mov_b32_e32 v31, v18
	v_mov_b32_e32 v32, v18
	v_mov_b32_e32 v33, v18
	v_lshlrev_b32_e32 v0, 4, v0
	v_or_b32_e32 v88, v104, v0
	s_waitcnt lgkmcnt(0)
	v_mfma_f32_32x32x16_f16 v[18:33], v[90:93], v[94:97], v[18:33]
	ds_read_b128 v[94:97], v85 offset:28672
	ds_read_b128 v[98:101], v88
	v_mov_b32_e32 v51, v50
	v_mov_b32_e32 v52, v50
	v_mov_b32_e32 v53, v50
	v_mov_b32_e32 v54, v50
	v_mov_b32_e32 v55, v50
	v_mov_b32_e32 v56, v50
	v_mov_b32_e32 v57, v50
	v_mov_b32_e32 v58, v50
	v_mov_b32_e32 v59, v50
	v_mov_b32_e32 v60, v50
	v_mov_b32_e32 v61, v50
	v_mov_b32_e32 v62, v50
	v_mov_b32_e32 v63, v50
	v_mov_b32_e32 v64, v50
	v_mov_b32_e32 v65, v50
	v_mov_b32_e32 v35, v34
	v_mov_b32_e32 v36, v34
	v_mov_b32_e32 v37, v34
	v_mov_b32_e32 v38, v34
	v_mov_b32_e32 v39, v34
	v_mov_b32_e32 v40, v34
	v_mov_b32_e32 v41, v34
	v_mov_b32_e32 v42, v34
	v_mov_b32_e32 v43, v34
	v_mov_b32_e32 v44, v34
	v_mov_b32_e32 v45, v34
	v_mov_b32_e32 v46, v34
	v_mov_b32_e32 v47, v34
	v_mov_b32_e32 v48, v34
	v_mov_b32_e32 v49, v34
	v_mfma_f32_32x32x16_f16 v[50:65], v[90:93], v[6:9], v[50:65]
	v_mov_b32_e32 v3, v2
	v_mov_b32_e32 v4, v2
	v_mov_b32_e32 v5, v2
	v_mov_b32_e32 v6, v2
	v_mov_b32_e32 v7, v2
	v_mov_b32_e32 v8, v2
	v_mov_b32_e32 v9, v2
	v_mfma_f32_32x32x16_f16 v[34:49], v[90:93], v[10:13], v[34:49]
	v_mov_b32_e32 v10, v2
	v_mov_b32_e32 v11, v2
	v_mov_b32_e32 v12, v2
	v_mov_b32_e32 v13, v2
	v_mov_b32_e32 v14, v2
	v_mov_b32_e32 v15, v2
	v_mov_b32_e32 v16, v2
	v_mov_b32_e32 v17, v2
	v_or_b32_e32 v0, v105, v0
	v_bitop3_b32 v87, v84, v106, 4 bitop3:0x36
	s_waitcnt lgkmcnt(0)
	v_mfma_f32_32x32x16_f16 v[2:17], v[90:93], v[94:97], v[2:17]
	ds_read_b128 v[90:93], v0 offset:16384
	ds_read_b128 v[94:97], v0 offset:20480
	v_lshlrev_b32_e32 v87, 4, v87
	v_or_b32_e32 v89, v104, v87
	v_or_b32_e32 v87, v105, v87
	s_mov_b64 s[20:21], 0x100
	s_mov_b32 m0, s9
	s_cmpk_gt_u32 s0, 0x2a98
	s_waitcnt lgkmcnt(0)
	v_mfma_f32_32x32x16_f16 v[50:65], v[98:101], v[90:93], v[50:65]
	v_mfma_f32_32x32x16_f16 v[34:49], v[98:101], v[94:97], v[34:49]
	ds_read_b128 v[90:93], v0 offset:24576
	ds_read_b128 v[94:97], v0 offset:28672
	s_waitcnt lgkmcnt(0)
	v_mfma_f32_32x32x16_f16 v[18:33], v[98:101], v[90:93], v[18:33]
	v_bitop3_b32 v90, v84, v106, 6 bitop3:0x36
	v_lshlrev_b32_e32 v90, 4, v90
	v_or_b32_e32 v91, v104, v90
	v_or_b32_e32 v90, v105, v90
	v_mfma_f32_32x32x16_f16 v[2:17], v[98:101], v[94:97], v[2:17]
	ds_read_b128 v[92:95], v89
	ds_read_b128 v[96:99], v87 offset:16384
	s_waitcnt lgkmcnt(0)
	v_mfma_f32_32x32x16_f16 v[50:65], v[92:95], v[96:99], v[50:65]
	ds_read_b128 v[96:99], v87 offset:20480
	ds_read_b128 v[100:103], v87 offset:24576
	s_waitcnt lgkmcnt(0)
	v_mfma_f32_32x32x16_f16 v[34:49], v[92:95], v[96:99], v[34:49]
	ds_read_b128 v[96:99], v87 offset:28672
	v_mfma_f32_32x32x16_f16 v[18:33], v[92:95], v[100:103], v[18:33]
	ds_read_b128 v[100:103], v91
	s_waitcnt lgkmcnt(0)
	v_mfma_f32_32x32x16_f16 v[2:17], v[92:95], v[96:99], v[2:17]
	ds_read_b128 v[92:95], v90 offset:16384
	ds_read_b128 v[96:99], v90 offset:20480
	s_waitcnt lgkmcnt(1)
	v_mfma_f32_32x32x16_f16 v[50:65], v[100:103], v[92:95], v[50:65]
	s_waitcnt lgkmcnt(0)
	v_mfma_f32_32x32x16_f16 v[34:49], v[100:103], v[96:99], v[34:49]
	ds_read_b128 v[92:95], v90 offset:24576
	ds_read_b128 v[96:99], v90 offset:28672
	s_waitcnt vmcnt(0) lgkmcnt(0)
	s_barrier
	v_mfma_f32_32x32x16_f16 v[18:33], v[100:103], v[92:95], v[18:33]
	v_lshl_add_u64 v[92:93], v[68:69], 0, s[20:21]
	global_load_lds_dwordx4 v[92:93], off
	v_lshl_add_u64 v[92:93], v[70:71], 0, s[20:21]
	s_mov_b32 m0, s12
	s_nop 0
	global_load_lds_dwordx4 v[92:93], off
	v_lshl_add_u64 v[92:93], v[72:73], 0, s[20:21]
	s_mov_b32 m0, s13
	v_mfma_f32_32x32x16_f16 v[2:17], v[100:103], v[96:99], v[2:17]
	global_load_lds_dwordx4 v[92:93], off
	v_lshl_add_u64 v[92:93], v[74:75], 0, s[20:21]
	s_mov_b32 m0, s14
	s_nop 0
	global_load_lds_dwordx4 v[92:93], off
	v_lshl_add_u64 v[92:93], v[76:77], 0, s[20:21]
	s_mov_b32 m0, s15
	s_nop 0
	global_load_lds_dwordx4 v[92:93], off
	v_lshl_add_u64 v[92:93], v[78:79], 0, s[20:21]
	s_mov_b32 m0, s16
	s_nop 0
	global_load_lds_dwordx4 v[92:93], off
	v_lshl_add_u64 v[92:93], v[80:81], 0, s[20:21]
	s_mov_b32 m0, s17
	s_nop 0
	global_load_lds_dwordx4 v[92:93], off
	v_lshl_add_u64 v[92:93], v[82:83], 0, s[20:21]
	s_mov_b32 m0, s18
	s_mov_b64 s[20:21], 0x180
	global_load_lds_dwordx4 v[92:93], off
	ds_read_b128 v[92:95], v86 offset:32768
	ds_read_b128 v[96:99], v85 offset:49152
	s_waitcnt lgkmcnt(0)
	v_mfma_f32_32x32x16_f16 v[50:65], v[92:95], v[96:99], v[50:65]
	ds_read_b128 v[96:99], v85 offset:53248
	ds_read_b128 v[100:103], v85 offset:57344
	s_mov_b32 m0, s1
	s_waitcnt lgkmcnt(1)
	v_mfma_f32_32x32x16_f16 v[34:49], v[92:95], v[96:99], v[34:49]
	s_waitcnt lgkmcnt(0)
	v_mfma_f32_32x32x16_f16 v[18:33], v[92:95], v[100:103], v[18:33]
	ds_read_b128 v[96:99], v85 offset:61440
	ds_read_b128 v[100:103], v88 offset:32768
	s_waitcnt lgkmcnt(1)
	v_mfma_f32_32x32x16_f16 v[2:17], v[92:95], v[96:99], v[2:17]
	ds_read_b128 v[92:95], v0 offset:49152
	ds_read_b128 v[96:99], v0 offset:53248
	s_waitcnt lgkmcnt(1)
	v_mfma_f32_32x32x16_f16 v[50:65], v[100:103], v[92:95], v[50:65]
	s_waitcnt lgkmcnt(0)
	v_mfma_f32_32x32x16_f16 v[34:49], v[100:103], v[96:99], v[34:49]
	ds_read_b128 v[92:95], v0 offset:57344
	ds_read_b128 v[96:99], v0 offset:61440
	s_waitcnt lgkmcnt(1)
	v_mfma_f32_32x32x16_f16 v[18:33], v[100:103], v[92:95], v[18:33]
	s_waitcnt lgkmcnt(0)
	v_mfma_f32_32x32x16_f16 v[2:17], v[100:103], v[96:99], v[2:17]
	ds_read_b128 v[92:95], v89 offset:32768
	ds_read_b128 v[96:99], v87 offset:49152
	s_waitcnt lgkmcnt(0)
	v_mfma_f32_32x32x16_f16 v[50:65], v[92:95], v[96:99], v[50:65]
	ds_read_b128 v[96:99], v87 offset:53248
	ds_read_b128 v[100:103], v87 offset:57344
	s_waitcnt lgkmcnt(1)
	v_mfma_f32_32x32x16_f16 v[34:49], v[92:95], v[96:99], v[34:49]
	s_waitcnt lgkmcnt(0)
	v_mfma_f32_32x32x16_f16 v[18:33], v[92:95], v[100:103], v[18:33]
	ds_read_b128 v[96:99], v87 offset:61440
	ds_read_b128 v[100:103], v91 offset:32768
	s_waitcnt lgkmcnt(1)
	v_mfma_f32_32x32x16_f16 v[2:17], v[92:95], v[96:99], v[2:17]
	ds_read_b128 v[92:95], v90 offset:49152
	ds_read_b128 v[96:99], v90 offset:53248
	s_waitcnt lgkmcnt(1)
	v_mfma_f32_32x32x16_f16 v[50:65], v[100:103], v[92:95], v[50:65]
	s_waitcnt lgkmcnt(0)
	v_mfma_f32_32x32x16_f16 v[34:49], v[100:103], v[96:99], v[34:49]
	ds_read_b128 v[92:95], v90 offset:57344
	ds_read_b128 v[96:99], v90 offset:61440
	s_waitcnt vmcnt(0) lgkmcnt(0)
	s_barrier
	v_mfma_f32_32x32x16_f16 v[18:33], v[100:103], v[92:95], v[18:33]
	v_lshl_add_u64 v[92:93], v[68:69], 0, s[20:21]
	global_load_lds_dwordx4 v[92:93], off
	v_lshl_add_u64 v[92:93], v[70:71], 0, s[20:21]
	s_mov_b32 m0, s2
	s_nop 0
	global_load_lds_dwordx4 v[92:93], off
	v_lshl_add_u64 v[92:93], v[72:73], 0, s[20:21]
	s_mov_b32 m0, s3
	v_mfma_f32_32x32x16_f16 v[2:17], v[100:103], v[96:99], v[2:17]
	global_load_lds_dwordx4 v[92:93], off
	v_lshl_add_u64 v[92:93], v[74:75], 0, s[20:21]
	s_mov_b32 m0, s4
	s_nop 0
	global_load_lds_dwordx4 v[92:93], off
	v_lshl_add_u64 v[92:93], v[76:77], 0, s[20:21]
	s_mov_b32 m0, s5
	s_nop 0
	global_load_lds_dwordx4 v[92:93], off
	v_lshl_add_u64 v[92:93], v[78:79], 0, s[20:21]
	s_mov_b32 m0, s6
	s_nop 0
	global_load_lds_dwordx4 v[92:93], off
	v_lshl_add_u64 v[92:93], v[80:81], 0, s[20:21]
	s_mov_b32 m0, s7
	s_nop 0
	global_load_lds_dwordx4 v[92:93], off
	v_lshl_add_u64 v[92:93], v[82:83], 0, s[20:21]
	s_mov_b32 m0, s8
	s_mov_b64 s[20:21], 0x200
	global_load_lds_dwordx4 v[92:93], off
	ds_read_b128 v[92:95], v86
	ds_read_b128 v[96:99], v85 offset:16384
	s_waitcnt lgkmcnt(0)
	v_mfma_f32_32x32x16_f16 v[50:65], v[92:95], v[96:99], v[50:65]
	ds_read_b128 v[96:99], v85 offset:20480
	ds_read_b128 v[100:103], v85 offset:24576
	s_mov_b32 m0, s9
	s_waitcnt lgkmcnt(1)
	v_mfma_f32_32x32x16_f16 v[34:49], v[92:95], v[96:99], v[34:49]
	s_waitcnt lgkmcnt(0)
	v_mfma_f32_32x32x16_f16 v[18:33], v[92:95], v[100:103], v[18:33]
	ds_read_b128 v[96:99], v85 offset:28672
	ds_read_b128 v[100:103], v88
	s_waitcnt lgkmcnt(1)
	v_mfma_f32_32x32x16_f16 v[2:17], v[92:95], v[96:99], v[2:17]
	ds_read_b128 v[92:95], v0 offset:16384
	ds_read_b128 v[96:99], v0 offset:20480
	s_waitcnt lgkmcnt(1)
	v_mfma_f32_32x32x16_f16 v[50:65], v[100:103], v[92:95], v[50:65]
	s_waitcnt lgkmcnt(0)
	v_mfma_f32_32x32x16_f16 v[34:49], v[100:103], v[96:99], v[34:49]
	ds_read_b128 v[92:95], v0 offset:24576
	ds_read_b128 v[96:99], v0 offset:28672
	s_waitcnt lgkmcnt(1)
	v_mfma_f32_32x32x16_f16 v[18:33], v[100:103], v[92:95], v[18:33]
	s_waitcnt lgkmcnt(0)
	v_mfma_f32_32x32x16_f16 v[2:17], v[100:103], v[96:99], v[2:17]
	ds_read_b128 v[92:95], v89
	ds_read_b128 v[96:99], v87 offset:16384
	s_waitcnt lgkmcnt(0)
	v_mfma_f32_32x32x16_f16 v[50:65], v[92:95], v[96:99], v[50:65]
	ds_read_b128 v[96:99], v87 offset:20480
	ds_read_b128 v[100:103], v87 offset:24576
	s_waitcnt lgkmcnt(1)
	v_mfma_f32_32x32x16_f16 v[34:49], v[92:95], v[96:99], v[34:49]
	s_waitcnt lgkmcnt(0)
	v_mfma_f32_32x32x16_f16 v[18:33], v[92:95], v[100:103], v[18:33]
	ds_read_b128 v[96:99], v87 offset:28672
	ds_read_b128 v[100:103], v91
	s_waitcnt lgkmcnt(1)
	v_mfma_f32_32x32x16_f16 v[2:17], v[92:95], v[96:99], v[2:17]
	ds_read_b128 v[92:95], v90 offset:16384
	ds_read_b128 v[96:99], v90 offset:20480
	s_waitcnt lgkmcnt(1)
	v_mfma_f32_32x32x16_f16 v[50:65], v[100:103], v[92:95], v[50:65]
	s_waitcnt lgkmcnt(0)
	v_mfma_f32_32x32x16_f16 v[34:49], v[100:103], v[96:99], v[34:49]
	ds_read_b128 v[92:95], v90 offset:24576
	ds_read_b128 v[96:99], v90 offset:28672
	s_waitcnt vmcnt(0) lgkmcnt(0)
	s_barrier
	v_mfma_f32_32x32x16_f16 v[18:33], v[100:103], v[92:95], v[18:33]
	v_lshl_add_u64 v[92:93], v[68:69], 0, s[20:21]
	global_load_lds_dwordx4 v[92:93], off
	v_lshl_add_u64 v[92:93], v[70:71], 0, s[20:21]
	s_mov_b32 m0, s12
	s_nop 0
	global_load_lds_dwordx4 v[92:93], off
	v_lshl_add_u64 v[92:93], v[72:73], 0, s[20:21]
	s_mov_b32 m0, s13
	v_mfma_f32_32x32x16_f16 v[2:17], v[100:103], v[96:99], v[2:17]
	global_load_lds_dwordx4 v[92:93], off
	v_lshl_add_u64 v[92:93], v[74:75], 0, s[20:21]
	s_mov_b32 m0, s14
	s_nop 0
	global_load_lds_dwordx4 v[92:93], off
	v_lshl_add_u64 v[92:93], v[76:77], 0, s[20:21]
	s_mov_b32 m0, s15
	s_nop 0
	global_load_lds_dwordx4 v[92:93], off
	v_lshl_add_u64 v[92:93], v[78:79], 0, s[20:21]
	s_mov_b32 m0, s16
	s_nop 0
	global_load_lds_dwordx4 v[92:93], off
	v_lshl_add_u64 v[92:93], v[80:81], 0, s[20:21]
	s_mov_b32 m0, s17
	s_nop 0
	global_load_lds_dwordx4 v[92:93], off
	v_lshl_add_u64 v[92:93], v[82:83], 0, s[20:21]
	s_mov_b32 m0, s18
	s_mov_b64 s[20:21], 0x280
	global_load_lds_dwordx4 v[92:93], off
	ds_read_b128 v[92:95], v86 offset:32768
	ds_read_b128 v[96:99], v85 offset:49152
	s_waitcnt lgkmcnt(0)
	v_mfma_f32_32x32x16_f16 v[50:65], v[92:95], v[96:99], v[50:65]
	ds_read_b128 v[96:99], v85 offset:53248
	ds_read_b128 v[100:103], v85 offset:57344
	s_mov_b32 m0, s1
	s_waitcnt lgkmcnt(1)
	v_mfma_f32_32x32x16_f16 v[34:49], v[92:95], v[96:99], v[34:49]
	s_waitcnt lgkmcnt(0)
	v_mfma_f32_32x32x16_f16 v[18:33], v[92:95], v[100:103], v[18:33]
	ds_read_b128 v[96:99], v85 offset:61440
	ds_read_b128 v[100:103], v88 offset:32768
	s_waitcnt lgkmcnt(1)
	v_mfma_f32_32x32x16_f16 v[2:17], v[92:95], v[96:99], v[2:17]
	ds_read_b128 v[92:95], v0 offset:49152
	ds_read_b128 v[96:99], v0 offset:53248
	s_waitcnt lgkmcnt(1)
	v_mfma_f32_32x32x16_f16 v[50:65], v[100:103], v[92:95], v[50:65]
	s_waitcnt lgkmcnt(0)
	v_mfma_f32_32x32x16_f16 v[34:49], v[100:103], v[96:99], v[34:49]
	ds_read_b128 v[92:95], v0 offset:57344
	ds_read_b128 v[96:99], v0 offset:61440
	s_waitcnt lgkmcnt(1)
	v_mfma_f32_32x32x16_f16 v[18:33], v[100:103], v[92:95], v[18:33]
	s_waitcnt lgkmcnt(0)
	v_mfma_f32_32x32x16_f16 v[2:17], v[100:103], v[96:99], v[2:17]
	ds_read_b128 v[92:95], v89 offset:32768
	ds_read_b128 v[96:99], v87 offset:49152
	s_waitcnt lgkmcnt(0)
	v_mfma_f32_32x32x16_f16 v[50:65], v[92:95], v[96:99], v[50:65]
	ds_read_b128 v[96:99], v87 offset:53248
	ds_read_b128 v[100:103], v87 offset:57344
	s_waitcnt lgkmcnt(1)
	v_mfma_f32_32x32x16_f16 v[34:49], v[92:95], v[96:99], v[34:49]
	s_waitcnt lgkmcnt(0)
	v_mfma_f32_32x32x16_f16 v[18:33], v[92:95], v[100:103], v[18:33]
	ds_read_b128 v[96:99], v87 offset:61440
	ds_read_b128 v[100:103], v91 offset:32768
	s_waitcnt lgkmcnt(1)
	v_mfma_f32_32x32x16_f16 v[2:17], v[92:95], v[96:99], v[2:17]
	ds_read_b128 v[92:95], v90 offset:49152
	ds_read_b128 v[96:99], v90 offset:53248
	s_waitcnt lgkmcnt(1)
	v_mfma_f32_32x32x16_f16 v[50:65], v[100:103], v[92:95], v[50:65]
	s_waitcnt lgkmcnt(0)
	v_mfma_f32_32x32x16_f16 v[34:49], v[100:103], v[96:99], v[34:49]
	ds_read_b128 v[92:95], v90 offset:57344
	ds_read_b128 v[96:99], v90 offset:61440
	s_waitcnt vmcnt(0) lgkmcnt(0)
	s_barrier
	v_mfma_f32_32x32x16_f16 v[18:33], v[100:103], v[92:95], v[18:33]
	v_lshl_add_u64 v[92:93], v[68:69], 0, s[20:21]
	global_load_lds_dwordx4 v[92:93], off
	v_lshl_add_u64 v[92:93], v[70:71], 0, s[20:21]
	s_mov_b32 m0, s2
	s_nop 0
	global_load_lds_dwordx4 v[92:93], off
	v_lshl_add_u64 v[92:93], v[72:73], 0, s[20:21]
	s_mov_b32 m0, s3
	v_mfma_f32_32x32x16_f16 v[2:17], v[100:103], v[96:99], v[2:17]
	global_load_lds_dwordx4 v[92:93], off
	v_lshl_add_u64 v[92:93], v[74:75], 0, s[20:21]
	s_mov_b32 m0, s4
	s_nop 0
	global_load_lds_dwordx4 v[92:93], off
	v_lshl_add_u64 v[92:93], v[76:77], 0, s[20:21]
	s_mov_b32 m0, s5
	s_nop 0
	global_load_lds_dwordx4 v[92:93], off
	v_lshl_add_u64 v[92:93], v[78:79], 0, s[20:21]
	s_mov_b32 m0, s6
	s_nop 0
	global_load_lds_dwordx4 v[92:93], off
	v_lshl_add_u64 v[92:93], v[80:81], 0, s[20:21]
	s_mov_b32 m0, s7
	s_nop 0
	global_load_lds_dwordx4 v[92:93], off
	v_lshl_add_u64 v[92:93], v[82:83], 0, s[20:21]
	s_mov_b32 m0, s8
	s_mov_b64 s[20:21], 0x300
	global_load_lds_dwordx4 v[92:93], off
	ds_read_b128 v[92:95], v86
	ds_read_b128 v[96:99], v85 offset:16384
	s_waitcnt lgkmcnt(0)
	v_mfma_f32_32x32x16_f16 v[50:65], v[92:95], v[96:99], v[50:65]
	ds_read_b128 v[96:99], v85 offset:20480
	ds_read_b128 v[100:103], v85 offset:24576
	s_mov_b32 m0, s9
	s_waitcnt lgkmcnt(1)
	v_mfma_f32_32x32x16_f16 v[34:49], v[92:95], v[96:99], v[34:49]
	s_waitcnt lgkmcnt(0)
	v_mfma_f32_32x32x16_f16 v[18:33], v[92:95], v[100:103], v[18:33]
	ds_read_b128 v[96:99], v85 offset:28672
	ds_read_b128 v[100:103], v88
	s_waitcnt lgkmcnt(1)
	v_mfma_f32_32x32x16_f16 v[2:17], v[92:95], v[96:99], v[2:17]
	ds_read_b128 v[92:95], v0 offset:16384
	ds_read_b128 v[96:99], v0 offset:20480
	s_waitcnt lgkmcnt(1)
	v_mfma_f32_32x32x16_f16 v[50:65], v[100:103], v[92:95], v[50:65]
	s_waitcnt lgkmcnt(0)
	v_mfma_f32_32x32x16_f16 v[34:49], v[100:103], v[96:99], v[34:49]
	ds_read_b128 v[92:95], v0 offset:24576
	ds_read_b128 v[96:99], v0 offset:28672
	s_waitcnt lgkmcnt(1)
	v_mfma_f32_32x32x16_f16 v[18:33], v[100:103], v[92:95], v[18:33]
	s_waitcnt lgkmcnt(0)
	v_mfma_f32_32x32x16_f16 v[2:17], v[100:103], v[96:99], v[2:17]
	ds_read_b128 v[92:95], v89
	ds_read_b128 v[96:99], v87 offset:16384
	s_waitcnt lgkmcnt(0)
	v_mfma_f32_32x32x16_f16 v[50:65], v[92:95], v[96:99], v[50:65]
	ds_read_b128 v[96:99], v87 offset:20480
	ds_read_b128 v[100:103], v87 offset:24576
	s_waitcnt lgkmcnt(1)
	v_mfma_f32_32x32x16_f16 v[34:49], v[92:95], v[96:99], v[34:49]
	s_waitcnt lgkmcnt(0)
	v_mfma_f32_32x32x16_f16 v[18:33], v[92:95], v[100:103], v[18:33]
	ds_read_b128 v[96:99], v87 offset:28672
	ds_read_b128 v[100:103], v91
	s_waitcnt lgkmcnt(1)
	v_mfma_f32_32x32x16_f16 v[2:17], v[92:95], v[96:99], v[2:17]
	ds_read_b128 v[92:95], v90 offset:16384
	ds_read_b128 v[96:99], v90 offset:20480
	s_waitcnt lgkmcnt(1)
	v_mfma_f32_32x32x16_f16 v[50:65], v[100:103], v[92:95], v[50:65]
	s_waitcnt lgkmcnt(0)
	v_mfma_f32_32x32x16_f16 v[34:49], v[100:103], v[96:99], v[34:49]
	ds_read_b128 v[92:95], v90 offset:24576
	ds_read_b128 v[96:99], v90 offset:28672
	s_waitcnt vmcnt(0) lgkmcnt(0)
	s_barrier
	v_mfma_f32_32x32x16_f16 v[18:33], v[100:103], v[92:95], v[18:33]
	v_lshl_add_u64 v[92:93], v[68:69], 0, s[20:21]
	global_load_lds_dwordx4 v[92:93], off
	v_lshl_add_u64 v[92:93], v[70:71], 0, s[20:21]
	s_mov_b32 m0, s12
	s_nop 0
	global_load_lds_dwordx4 v[92:93], off
	v_lshl_add_u64 v[92:93], v[72:73], 0, s[20:21]
	s_mov_b32 m0, s13
	v_mfma_f32_32x32x16_f16 v[2:17], v[100:103], v[96:99], v[2:17]
	global_load_lds_dwordx4 v[92:93], off
	v_lshl_add_u64 v[92:93], v[74:75], 0, s[20:21]
	s_mov_b32 m0, s14
	s_mov_b64 s[12:13], 0x380
	global_load_lds_dwordx4 v[92:93], off
	v_lshl_add_u64 v[92:93], v[76:77], 0, s[20:21]
	s_mov_b32 m0, s15
	v_lshl_add_u64 v[68:69], v[68:69], 0, s[12:13]
	global_load_lds_dwordx4 v[92:93], off
	v_lshl_add_u64 v[92:93], v[78:79], 0, s[20:21]
	s_mov_b32 m0, s16
	s_nop 0
	global_load_lds_dwordx4 v[92:93], off
	v_lshl_add_u64 v[92:93], v[80:81], 0, s[20:21]
	s_mov_b32 m0, s17
	s_nop 0
	global_load_lds_dwordx4 v[92:93], off
	v_lshl_add_u64 v[92:93], v[82:83], 0, s[20:21]
	s_mov_b32 m0, s18
	s_nop 0
	global_load_lds_dwordx4 v[92:93], off
	ds_read_b128 v[92:95], v86 offset:32768
	ds_read_b128 v[96:99], v85 offset:49152
	s_waitcnt lgkmcnt(0)
	v_mfma_f32_32x32x16_f16 v[50:65], v[92:95], v[96:99], v[50:65]
	ds_read_b128 v[96:99], v85 offset:53248
	ds_read_b128 v[100:103], v85 offset:57344
	s_mov_b32 m0, s1
	s_waitcnt lgkmcnt(1)
	v_mfma_f32_32x32x16_f16 v[34:49], v[92:95], v[96:99], v[34:49]
	s_waitcnt lgkmcnt(0)
	v_mfma_f32_32x32x16_f16 v[18:33], v[92:95], v[100:103], v[18:33]
	ds_read_b128 v[96:99], v85 offset:61440
	ds_read_b128 v[100:103], v88 offset:32768
	s_waitcnt lgkmcnt(1)
	v_mfma_f32_32x32x16_f16 v[2:17], v[92:95], v[96:99], v[2:17]
	ds_read_b128 v[92:95], v0 offset:49152
	ds_read_b128 v[96:99], v0 offset:53248
	s_waitcnt lgkmcnt(1)
	v_mfma_f32_32x32x16_f16 v[50:65], v[100:103], v[92:95], v[50:65]
	s_waitcnt lgkmcnt(0)
	v_mfma_f32_32x32x16_f16 v[34:49], v[100:103], v[96:99], v[34:49]
	ds_read_b128 v[92:95], v0 offset:57344
	ds_read_b128 v[96:99], v0 offset:61440
	s_waitcnt lgkmcnt(1)
	v_mfma_f32_32x32x16_f16 v[18:33], v[100:103], v[92:95], v[18:33]
	s_waitcnt lgkmcnt(0)
	v_mfma_f32_32x32x16_f16 v[2:17], v[100:103], v[96:99], v[2:17]
	ds_read_b128 v[92:95], v89 offset:32768
	ds_read_b128 v[96:99], v87 offset:49152
	s_waitcnt lgkmcnt(0)
	v_mfma_f32_32x32x16_f16 v[50:65], v[92:95], v[96:99], v[50:65]
	ds_read_b128 v[96:99], v87 offset:53248
	ds_read_b128 v[100:103], v87 offset:57344
	s_waitcnt lgkmcnt(1)
	v_mfma_f32_32x32x16_f16 v[34:49], v[92:95], v[96:99], v[34:49]
	s_waitcnt lgkmcnt(0)
	v_mfma_f32_32x32x16_f16 v[18:33], v[92:95], v[100:103], v[18:33]
	ds_read_b128 v[96:99], v87 offset:61440
	ds_read_b128 v[100:103], v91 offset:32768
	s_waitcnt lgkmcnt(1)
	v_mfma_f32_32x32x16_f16 v[2:17], v[92:95], v[96:99], v[2:17]
	ds_read_b128 v[92:95], v90 offset:49152
	ds_read_b128 v[96:99], v90 offset:53248
	s_waitcnt lgkmcnt(1)
	v_mfma_f32_32x32x16_f16 v[50:65], v[100:103], v[92:95], v[50:65]
	s_waitcnt lgkmcnt(0)
	v_mfma_f32_32x32x16_f16 v[34:49], v[100:103], v[96:99], v[34:49]
	ds_read_b128 v[92:95], v90 offset:57344
	ds_read_b128 v[96:99], v90 offset:61440
	s_waitcnt vmcnt(0) lgkmcnt(0)
	s_barrier
	global_load_lds_dwordx4 v[68:69], off
	v_lshl_add_u64 v[68:69], v[70:71], 0, s[12:13]
	s_mov_b32 m0, s2
	v_mfma_f32_32x32x16_f16 v[18:33], v[100:103], v[92:95], v[18:33]
	global_load_lds_dwordx4 v[68:69], off
	v_lshl_add_u64 v[68:69], v[72:73], 0, s[12:13]
	s_mov_b32 m0, s3
	s_cselect_b64 s[2:3], -1, 0
	global_load_lds_dwordx4 v[68:69], off
	v_lshl_add_u64 v[68:69], v[74:75], 0, s[12:13]
	s_mov_b32 m0, s4
	v_mfma_f32_32x32x16_f16 v[2:17], v[100:103], v[96:99], v[2:17]
	global_load_lds_dwordx4 v[68:69], off
	v_lshl_add_u64 v[68:69], v[76:77], 0, s[12:13]
	s_mov_b32 m0, s5
	s_cmpk_lt_u32 s0, 0x2a99
	global_load_lds_dwordx4 v[68:69], off
	v_lshl_add_u64 v[68:69], v[78:79], 0, s[12:13]
	s_mov_b32 m0, s6
	s_nop 0
	global_load_lds_dwordx4 v[68:69], off
	v_lshl_add_u64 v[68:69], v[80:81], 0, s[12:13]
	s_mov_b32 m0, s7
	s_nop 0
	global_load_lds_dwordx4 v[68:69], off
	v_lshl_add_u64 v[68:69], v[82:83], 0, s[12:13]
	s_mov_b32 m0, s8
	s_nop 0
	global_load_lds_dwordx4 v[68:69], off
	ds_read_b128 v[68:71], v86
	ds_read_b128 v[72:75], v85 offset:16384
	s_waitcnt lgkmcnt(0)
	v_mfma_f32_32x32x16_f16 v[50:65], v[68:71], v[72:75], v[50:65]
	ds_read_b128 v[72:75], v85 offset:20480
	ds_read_b128 v[76:79], v85 offset:24576
	s_waitcnt lgkmcnt(1)
	v_mfma_f32_32x32x16_f16 v[34:49], v[68:71], v[72:75], v[34:49]
	s_waitcnt lgkmcnt(0)
	v_mfma_f32_32x32x16_f16 v[18:33], v[68:71], v[76:79], v[18:33]
	ds_read_b128 v[72:75], v85 offset:28672
	ds_read_b128 v[76:79], v88
	s_waitcnt lgkmcnt(1)
	v_mfma_f32_32x32x16_f16 v[2:17], v[68:71], v[72:75], v[2:17]
	ds_read_b128 v[68:71], v0 offset:16384
	ds_read_b128 v[72:75], v0 offset:20480
	s_waitcnt lgkmcnt(1)
	v_mfma_f32_32x32x16_f16 v[50:65], v[76:79], v[68:71], v[50:65]
	s_waitcnt lgkmcnt(0)
	v_mfma_f32_32x32x16_f16 v[34:49], v[76:79], v[72:75], v[34:49]
	ds_read_b128 v[68:71], v0 offset:24576
	ds_read_b128 v[72:75], v0 offset:28672
	s_waitcnt lgkmcnt(1)
	v_mfma_f32_32x32x16_f16 v[18:33], v[76:79], v[68:71], v[18:33]
	s_waitcnt lgkmcnt(0)
	v_mfma_f32_32x32x16_f16 v[2:17], v[76:79], v[72:75], v[2:17]
	ds_read_b128 v[68:71], v89
	ds_read_b128 v[72:75], v87 offset:16384
	s_waitcnt lgkmcnt(0)
	v_mfma_f32_32x32x16_f16 v[50:65], v[68:71], v[72:75], v[50:65]
	ds_read_b128 v[72:75], v87 offset:20480
	ds_read_b128 v[76:79], v87 offset:24576
	s_waitcnt lgkmcnt(1)
	v_mfma_f32_32x32x16_f16 v[34:49], v[68:71], v[72:75], v[34:49]
	s_waitcnt lgkmcnt(0)
	v_mfma_f32_32x32x16_f16 v[18:33], v[68:71], v[76:79], v[18:33]
	ds_read_b128 v[72:75], v87 offset:28672
	ds_read_b128 v[76:79], v91
	s_waitcnt lgkmcnt(1)
	v_mfma_f32_32x32x16_f16 v[2:17], v[68:71], v[72:75], v[2:17]
	ds_read_b128 v[68:71], v90 offset:16384
	ds_read_b128 v[72:75], v90 offset:20480
	s_waitcnt lgkmcnt(1)
	v_mfma_f32_32x32x16_f16 v[50:65], v[76:79], v[68:71], v[50:65]
	s_waitcnt lgkmcnt(0)
	v_mfma_f32_32x32x16_f16 v[34:49], v[76:79], v[72:75], v[34:49]
	ds_read_b128 v[68:71], v90 offset:24576
	ds_read_b128 v[72:75], v90 offset:28672
	s_waitcnt vmcnt(0) lgkmcnt(0)
	s_barrier
	v_mfma_f32_32x32x16_f16 v[18:33], v[76:79], v[68:71], v[18:33]
	v_mfma_f32_32x32x16_f16 v[2:17], v[76:79], v[72:75], v[2:17]
	ds_read_b128 v[68:71], v86 offset:32768
	ds_read_b128 v[72:75], v85 offset:49152
	s_waitcnt lgkmcnt(0)
	v_mfma_f32_32x32x16_f16 v[50:65], v[68:71], v[72:75], v[50:65]
	ds_read_b128 v[72:75], v85 offset:53248
	s_waitcnt lgkmcnt(0)
	v_mfma_f32_32x32x16_f16 v[34:49], v[68:71], v[72:75], v[34:49]
	ds_read_b128 v[72:75], v85 offset:57344
	s_waitcnt lgkmcnt(0)
	v_mfma_f32_32x32x16_f16 v[18:33], v[68:71], v[72:75], v[18:33]
	ds_read_b128 v[72:75], v85 offset:61440
	s_waitcnt lgkmcnt(0)
	v_mfma_f32_32x32x16_f16 v[2:17], v[68:71], v[72:75], v[2:17]
	ds_read_b128 v[68:71], v88 offset:32768
	ds_read_b128 v[72:75], v0 offset:49152
	s_waitcnt lgkmcnt(0)
	v_mfma_f32_32x32x16_f16 v[50:65], v[68:71], v[72:75], v[50:65]
	ds_read_b128 v[72:75], v0 offset:53248
	s_waitcnt lgkmcnt(0)
	v_mfma_f32_32x32x16_f16 v[34:49], v[68:71], v[72:75], v[34:49]
	ds_read_b128 v[72:75], v0 offset:57344
	s_waitcnt lgkmcnt(0)
	v_mfma_f32_32x32x16_f16 v[18:33], v[68:71], v[72:75], v[18:33]
	ds_read_b128 v[72:75], v0 offset:61440
	s_waitcnt lgkmcnt(0)
	v_mfma_f32_32x32x16_f16 v[2:17], v[68:71], v[72:75], v[2:17]
	ds_read_b128 v[68:71], v89 offset:32768
	ds_read_b128 v[72:75], v87 offset:49152
	s_waitcnt lgkmcnt(0)
	v_mfma_f32_32x32x16_f16 v[50:65], v[68:71], v[72:75], v[50:65]
	ds_read_b128 v[72:75], v87 offset:53248
	s_waitcnt lgkmcnt(0)
	v_mfma_f32_32x32x16_f16 v[34:49], v[68:71], v[72:75], v[34:49]
	ds_read_b128 v[72:75], v87 offset:57344
	s_waitcnt lgkmcnt(0)
	v_mfma_f32_32x32x16_f16 v[18:33], v[68:71], v[72:75], v[18:33]
	ds_read_b128 v[72:75], v87 offset:61440
	s_waitcnt lgkmcnt(0)
	v_mfma_f32_32x32x16_f16 v[2:17], v[68:71], v[72:75], v[2:17]
	ds_read_b128 v[70:73], v91 offset:32768
	ds_read_b128 v[74:77], v90 offset:49152
	v_or_b32_e32 v68, s0, v1
	v_lshl_or_b32 v0, v84, 2, v68
	v_mov_b32_e32 v1, v67
	v_lshlrev_b64 v[0:1], 11, v[0:1]
	v_lshl_add_u64 v[0:1], s[10:11], 0, v[0:1]
	v_lshl_add_u64 v[0:1], v[0:1], 0, v[66:67]
	s_waitcnt lgkmcnt(0)
	v_mfma_f32_32x32x16_f16 v[50:65], v[70:73], v[74:77], v[50:65]
	ds_read_b128 v[74:77], v90 offset:53248
	s_mov_b64 s[0:1], -1
	s_waitcnt lgkmcnt(0)
	v_mfma_f32_32x32x16_f16 v[34:49], v[70:73], v[74:77], v[34:49]
	ds_read_b128 v[74:77], v90 offset:61440
	ds_read_b128 v[78:81], v90 offset:57344
	s_waitcnt lgkmcnt(0)
	s_barrier
	v_mfma_f32_32x32x16_f16 v[18:33], v[70:73], v[78:81], v[18:33]
	v_mfma_f32_32x32x16_f16 v[2:17], v[70:73], v[74:77], v[2:17]
	s_cbranch_scc1 .LBB4_10
	s_movk_i32 s4, 0x2b18
	v_cmp_gt_u32_e32 vcc, s4, v68
	s_and_saveexec_b64 s[0:1], vcc
	s_cbranch_execz .LBB4_3
	v_add_co_u32_e32 v66, vcc, 0x1000, v0
	global_store_dword v[0:1], v50, off nt
	global_store_dword v[0:1], v51, off offset:2048 nt
	v_addc_co_u32_e32 v67, vcc, 0, v1, vcc
	global_store_dword v[66:67], v52, off nt
	global_store_dword v[66:67], v53, off offset:2048 nt
